# forgetting attention steady tile step written by hand (running max folded into the score init, both sub-tiles' CF reads and the second sub-tile's K reads issued ahead) on top of the store-widening ver
# speedup vs baseline: 1.0006x; 1.0006x over previous
; __device__ __forceinline__ float max2_raw(float a, float b) { float d; asm("v_max_f32 %0, %1, %2" : "=v"(d) : "v"(a), "v"(b)); return d; }
; template <int MODE>
; __device__ __forceinline__ void attn_fox_sub(const bf16x8 (&qr)[4], f32x16& O0, f32x16& O1, float& m, float& l, unsigned saddr  , unsigned cfaddr  , int j, int kv0, int q, int hi) {
;     bf16x8 kf[4], vf[2][2]; f32x4 c0, c1, c2, c3;
;     asm volatile("ds_read_b128 %0, %12\n\tds_read_b128 %1, %12 offset:1024\n\tds_read_b128 %2, %12 offset:2048\n\tds_read_b128 %3, %12 offset:3072\n\t"
;                  "ds_read_b128 %4, %13\n\tds_read_b128 %5, %13 offset:1024\n\tds_read_b128 %6, %13 offset:2048\n\tds_read_b128 %7, %13 offset:3072\n\t"
;                  "ds_read_b128 %8, %14\n\tds_read_b128 %9, %14 offset:16\n\tds_read_b128 %10, %14 offset:64\n\tds_read_b128 %11, %14 offset:80\n\ts_waitcnt lgkmcnt(0)"
;                  : "=&v"(kf[0]), "=&v"(kf[1]), "=&v"(kf[2]), "=&v"(kf[3]), "=&v"(vf[0][0]), "=&v"(vf[0][1]), "=&v"(vf[1][0]), "=&v"(vf[1][1]), "=&v"(c0), "=&v"(c1), "=&v"(c2), "=&v"(c3)
;                  : "v"(saddr + (unsigned)j * 4096u), "v"(saddr + 8192u + (unsigned)j * 4096u), "v"(cfaddr) : "memory");
;     f32x16 S;
;     S[0] = c0[0]; S[1] = c0[1]; S[2] = c0[2]; S[3] = c0[3]; S[4] = c1[0]; S[5] = c1[1]; S[6] = c1[2]; S[7] = c1[3];
;     S[8] = c2[0]; S[9] = c2[1]; S[10] = c2[2]; S[11] = c2[3]; S[12] = c3[0]; S[13] = c3[1]; S[14] = c3[2]; S[15] = c3[3];
; #pragma unroll
;     for (int d0 = 0; d0 < 4; ++d0) S = __builtin_amdgcn_mfma_f32_32x32x16_bf16(kf[d0], qr[d0], S, 0, 0, 0);
;     if (MODE == 1) {
; #pragma unroll
;         for (int r = 0; r < 16; ++r) { const int key = kv0 + (r & 7) + 8 * hi + 16 * (r >> 3); if (key > q) S[r] = -INFINITY; }
;     }
;     float rm = rowmax16_raw(S);
;     { const auto rr = __builtin_amdgcn_permlane32_swap(__float_as_uint(rm), __float_as_uint(rm), false, false); rm = max2_raw(__uint_as_float(rr[0]), __uint_as_float(rr[1])); }
;     if (__any(rm > m)) {
;         const float mn = fmaxf(fmaxf(m, rm), -1e30f); const float alpha = __builtin_amdgcn_exp2f(m - mn);
;         l *= alpha; O0 *= alpha; O1 *= alpha; m = mn; }
;     float p[16]; float ps = 0.f;
; #pragma unroll
;     for (int r = 0; r < 16; ++r) { p[r] = __builtin_amdgcn_exp2f(S[r] - m); ps += p[r]; }
;     l += ps;
.LBB0_552:
	s_add_i32 s0, s0, 3
	s_cmp_gt_i32 s0, s14
	s_cbranch_scc1 .LBB0_542
	v_lshl_add_u32 v131, s15, 14, v149
	s_cmp_lg_u32 s16, s91
	s_mov_b64 s[0:1], -1
	s_cbranch_scc0 .LBB0_559
	v_add_u32_e32 v206, 0x1000, v131
	v_add_u32_e32 v211, 0x80, v153
	v_add_u32_e32 v207, 0x3000, v131
	v_add_u32_e32 v210, 0x2000, v131
	ds_read_b128 v[32:35], v206
	ds_read_b128 v[36:39], v206 offset:1024
	ds_read_b128 v[40:43], v206 offset:2048
	ds_read_b128 v[44:47], v206 offset:3072
	ds_read_b128 v[64:67], v211
	ds_read_b128 v[68:71], v211 offset:16
	ds_read_b128 v[72:75], v211 offset:64
	ds_read_b128 v[76:79], v211 offset:80
	ds_read_b128 v[174:177], v153
	ds_read_b128 v[178:181], v153 offset:16
	ds_read_b128 v[182:185], v153 offset:64
	ds_read_b128 v[186:189], v153 offset:80
	ds_read_b128 v[108:111], v207
	ds_read_b128 v[100:103], v207 offset:1024
	ds_read_b128 v[104:107], v207 offset:2048
	ds_read_b128 v[96:99], v207 offset:3072
	s_waitcnt lgkmcnt(8)
	v_pk_add_f32 v[64:65], v[64:65], v[154:155] op_sel_hi:[1,0] neg_lo:[0,1] neg_hi:[0,1]
	v_pk_add_f32 v[66:67], v[66:67], v[154:155] op_sel_hi:[1,0] neg_lo:[0,1] neg_hi:[0,1]
	v_pk_add_f32 v[68:69], v[68:69], v[154:155] op_sel_hi:[1,0] neg_lo:[0,1] neg_hi:[0,1]
	v_pk_add_f32 v[70:71], v[70:71], v[154:155] op_sel_hi:[1,0] neg_lo:[0,1] neg_hi:[0,1]
	v_pk_add_f32 v[72:73], v[72:73], v[154:155] op_sel_hi:[1,0] neg_lo:[0,1] neg_hi:[0,1]
	v_pk_add_f32 v[74:75], v[74:75], v[154:155] op_sel_hi:[1,0] neg_lo:[0,1] neg_hi:[0,1]
	v_pk_add_f32 v[76:77], v[76:77], v[154:155] op_sel_hi:[1,0] neg_lo:[0,1] neg_hi:[0,1]
	v_pk_add_f32 v[78:79], v[78:79], v[154:155] op_sel_hi:[1,0] neg_lo:[0,1] neg_hi:[0,1]
	s_nop 1
	v_mfma_f32_32x32x16_bf16 v[64:79], v[32:35], v[80:83], v[64:79]
	v_mfma_f32_32x32x16_bf16 v[64:79], v[36:39], v[84:87], v[64:79]
	v_mfma_f32_32x32x16_bf16 v[64:79], v[40:43], v[88:91], v[64:79]
	v_mfma_f32_32x32x16_bf16 v[64:79], v[44:47], v[92:95], v[64:79]
	ds_read_b128 v[158:161], v131
	ds_read_b128 v[162:165], v131 offset:1024
	ds_read_b128 v[166:169], v131 offset:2048
	ds_read_b128 v[170:173], v131 offset:3072
	s_waitcnt lgkmcnt(8)
	v_pk_add_f32 v[174:175], v[174:175], v[154:155] op_sel_hi:[1,0] neg_lo:[0,1] neg_hi:[0,1]
	v_pk_add_f32 v[176:177], v[176:177], v[154:155] op_sel_hi:[1,0] neg_lo:[0,1] neg_hi:[0,1]
	v_pk_add_f32 v[178:179], v[178:179], v[154:155] op_sel_hi:[1,0] neg_lo:[0,1] neg_hi:[0,1]
	v_pk_add_f32 v[180:181], v[180:181], v[154:155] op_sel_hi:[1,0] neg_lo:[0,1] neg_hi:[0,1]
	v_pk_add_f32 v[182:183], v[182:183], v[154:155] op_sel_hi:[1,0] neg_lo:[0,1] neg_hi:[0,1]
	v_pk_add_f32 v[184:185], v[184:185], v[154:155] op_sel_hi:[1,0] neg_lo:[0,1] neg_hi:[0,1]
	v_pk_add_f32 v[186:187], v[186:187], v[154:155] op_sel_hi:[1,0] neg_lo:[0,1] neg_hi:[0,1]
	v_pk_add_f32 v[188:189], v[188:189], v[154:155] op_sel_hi:[1,0] neg_lo:[0,1] neg_hi:[0,1]
	v_max3_f32 v200, v64, v65, v66
	v_max3_f32 v201, v67, v68, v69
	v_max3_f32 v202, v70, v71, v72
	v_max3_f32 v200, v200, v201, v202
	v_max3_f32 v201, v73, v74, v75
	v_max3_f32 v202, v76, v77, v78
	v_max3_f32 v201, v201, v202, v79
	v_max_f32_e32 v200, v200, v201
	v_mov_b32_e32 v201, v200
	s_nop 1
	v_permlane32_swap_b32_e32 v200, v201
	v_max_f32_e32 v201, v200, v201
	v_cmp_lt_f32_e32 vcc, 0, v201
	s_cbranch_vccz .Lfox_hot_1
	v_add_f32_e32 v201, v201, v154
	v_max3_f32 v205, v154, v201, s94
	v_sub_f32_e32 v204, v154, v205
	v_add_f32_e32 v64, v64, v204
	v_add_f32_e32 v65, v65, v204
	v_add_f32_e32 v66, v66, v204
	v_add_f32_e32 v67, v67, v204
	v_add_f32_e32 v68, v68, v204
	v_add_f32_e32 v69, v69, v204
	v_add_f32_e32 v70, v70, v204
	v_add_f32_e32 v71, v71, v204
	v_add_f32_e32 v72, v72, v204
	v_add_f32_e32 v73, v73, v204
	v_add_f32_e32 v74, v74, v204
	v_add_f32_e32 v75, v75, v204
	v_add_f32_e32 v76, v76, v204
	v_add_f32_e32 v77, v77, v204
	v_add_f32_e32 v78, v78, v204
	v_add_f32_e32 v79, v79, v204
	v_add_f32_e32 v174, v174, v204
	v_add_f32_e32 v175, v175, v204
	v_add_f32_e32 v176, v176, v204
	v_add_f32_e32 v177, v177, v204
	v_add_f32_e32 v178, v178, v204
	v_add_f32_e32 v179, v179, v204
	v_add_f32_e32 v180, v180, v204
	v_add_f32_e32 v181, v181, v204
	v_add_f32_e32 v182, v182, v204
	v_add_f32_e32 v183, v183, v204
	v_add_f32_e32 v184, v184, v204
	v_add_f32_e32 v185, v185, v204
	v_add_f32_e32 v186, v186, v204
	v_add_f32_e32 v187, v187, v204
	v_add_f32_e32 v188, v188, v204
	v_add_f32_e32 v189, v189, v204
	v_exp_f32_e32 v204, v204
	v_mov_b32_e32 v154, v205
	v_mul_f32_e32 v151, v151, v204
	v_pk_mul_f32 v[0:1], v[0:1], v[204:205] op_sel_hi:[1,0]
	v_pk_mul_f32 v[2:3], v[2:3], v[204:205] op_sel_hi:[1,0]
	v_pk_mul_f32 v[4:5], v[4:5], v[204:205] op_sel_hi:[1,0]
	v_pk_mul_f32 v[6:7], v[6:7], v[204:205] op_sel_hi:[1,0]
	v_pk_mul_f32 v[8:9], v[8:9], v[204:205] op_sel_hi:[1,0]
	v_pk_mul_f32 v[10:11], v[10:11], v[204:205] op_sel_hi:[1,0]
	v_pk_mul_f32 v[12:13], v[12:13], v[204:205] op_sel_hi:[1,0]
	v_pk_mul_f32 v[14:15], v[14:15], v[204:205] op_sel_hi:[1,0]
	v_pk_mul_f32 v[16:17], v[16:17], v[204:205] op_sel_hi:[1,0]
	v_pk_mul_f32 v[18:19], v[18:19], v[204:205] op_sel_hi:[1,0]
	v_pk_mul_f32 v[20:21], v[20:21], v[204:205] op_sel_hi:[1,0]
	v_pk_mul_f32 v[22:23], v[22:23], v[204:205] op_sel_hi:[1,0]
	v_pk_mul_f32 v[24:25], v[24:25], v[204:205] op_sel_hi:[1,0]
	v_pk_mul_f32 v[26:27], v[26:27], v[204:205] op_sel_hi:[1,0]
	v_pk_mul_f32 v[28:29], v[28:29], v[204:205] op_sel_hi:[1,0]
	v_pk_mul_f32 v[30:31], v[30:31], v[204:205] op_sel_hi:[1,0]
; __device__ __forceinline__ unsigned pk2(float lo, float hi) { const f32x2_pk v = {lo, hi}; return __builtin_bit_cast(unsigned, __builtin_convertvector(v, bf16x2)); }
; template <int MODE>
; __device__ __forceinline__ void attn_fox_sub(const bf16x8 (&qr)[4], f32x16& O0, f32x16& O1, float& m, float& l, unsigned saddr  , unsigned cfaddr  , int j, int kv0, int q, int hi) {
;     ...
;     float p[16]; float ps = 0.f;
; #pragma unroll
;     for (int r = 0; r < 16; ++r) { p[r] = __builtin_amdgcn_exp2f(S[r] - m); ps += p[r]; }
;     l += ps;
;     u32x4 w0, w1;
;     w0.x = pk2(p[0], p[1]); w0.y = pk2(p[2], p[3]); w0.z = pk2(p[4], p[5]); w0.w = pk2(p[6], p[7]);
;     w1.x = pk2(p[8], p[9]); w1.y = pk2(p[10], p[11]); w1.z = pk2(p[12], p[13]); w1.w = pk2(p[14], p[15]);
;     const bf16x8 pf0 = __builtin_bit_cast(bf16x8, w0), pf1 = __builtin_bit_cast(bf16x8, w1);
;     O0 = __builtin_amdgcn_mfma_f32_32x32x16_bf16(vf[0][0], pf0, O0, 0, 0, 0); O0 = __builtin_amdgcn_mfma_f32_32x32x16_bf16(vf[1][0], pf1, O0, 0, 0, 0);
;     O1 = __builtin_amdgcn_mfma_f32_32x32x16_bf16(vf[0][1], pf0, O1, 0, 0, 0); O1 = __builtin_amdgcn_mfma_f32_32x32x16_bf16(vf[1][1], pf1, O1, 0, 0, 0);
; __device__ __forceinline__ void attn_fox_unit(Frame& F, const bf16_t* Qh, const bf16_t* Kh, const bf16_t* Vth, const float* CFh, const int qb, bf16_t* AOp, const float k2max) {
;     ...
;                 if (jdiag == 1) { attn_fox_sub<1>(qr, O0, O1, m, l, sa, cf_a + 4u * (unsigned)(64 * T + 32), 1, 64 * T + 32, q, hi); attn_fox_sub<0>(qr, O0, O1, m, l, sa, cf_a + 4u * (unsigned)(64 * T), 0, 64 * T, q, hi); }
;                 else attn_fox_sub<1>(qr, O0, O1, m, l, sa, cf_a + 4u * (unsigned)(64 * T), 0, 64 * T, q, hi);
;             } else { attn_fox_sub<0>(qr, O0, O1, m, l, sa, cf_a + 4u * (unsigned)(64 * T + 32), 1, 64 * T + 32, q, hi); attn_fox_sub<0>(qr, O0, O1, m, l, sa, cf_a + 4u * (unsigned)(64 * T), 0, 64 * T, q, hi); }
.Lfox_hot_1:
	v_exp_f32_e32 v64, v64
	v_exp_f32_e32 v65, v65
	v_exp_f32_e32 v66, v66
	v_exp_f32_e32 v67, v67
	v_add_f32_e32 v203, 0, v64
	v_exp_f32_e32 v68, v68
	v_add_f32_e32 v203, v65, v203
	v_exp_f32_e32 v69, v69
	v_add_f32_e32 v203, v66, v203
	v_exp_f32_e32 v70, v70
	v_add_f32_e32 v203, v67, v203
	v_exp_f32_e32 v71, v71
	v_add_f32_e32 v203, v68, v203
	v_exp_f32_e32 v72, v72
	v_add_f32_e32 v203, v69, v203
	v_exp_f32_e32 v73, v73
	v_add_f32_e32 v203, v70, v203
	v_exp_f32_e32 v74, v74
	v_add_f32_e32 v203, v71, v203
	v_exp_f32_e32 v75, v75
	v_cvt_pk_bf16_f32 v64, v64, v65
	v_cvt_pk_bf16_f32 v65, v66, v67
	v_cvt_pk_bf16_f32 v66, v68, v69
	v_cvt_pk_bf16_f32 v67, v70, v71
	v_add_f32_e32 v203, v72, v203
	v_exp_f32_e32 v76, v76
	s_waitcnt lgkmcnt(4)
	v_mfma_f32_32x32x16_bf16 v[0:15], v[108:111], v[64:67], v[0:15]
	v_add_f32_e32 v203, v73, v203
	v_exp_f32_e32 v77, v77
	v_add_f32_e32 v203, v74, v203
	v_exp_f32_e32 v78, v78
	v_add_f32_e32 v203, v75, v203
	v_exp_f32_e32 v79, v79
	v_mfma_f32_32x32x16_bf16 v[16:31], v[100:103], v[64:67], v[16:31]
	v_add_f32_e32 v203, v76, v203
	v_add_f32_e32 v203, v77, v203
	v_add_f32_e32 v203, v78, v203
	v_add_f32_e32 v203, v79, v203
	v_cvt_pk_bf16_f32 v68, v72, v73
	v_cvt_pk_bf16_f32 v69, v74, v75
	v_cvt_pk_bf16_f32 v70, v76, v77
	v_cvt_pk_bf16_f32 v71, v78, v79
	v_add_f32_e32 v151, v151, v203
	s_nop 0
	v_mfma_f32_32x32x16_bf16 v[0:15], v[104:107], v[68:71], v[0:15]
	v_mfma_f32_32x32x16_bf16 v[16:31], v[96:99], v[68:71], v[16:31]
	ds_read_b128 v[108:111], v210
	ds_read_b128 v[100:103], v210 offset:1024
	ds_read_b128 v[104:107], v210 offset:2048
	ds_read_b128 v[96:99], v210 offset:3072
	s_waitcnt lgkmcnt(4)
	v_mfma_f32_32x32x16_bf16 v[174:189], v[158:161], v[80:83], v[174:189]
	v_mfma_f32_32x32x16_bf16 v[174:189], v[162:165], v[84:87], v[174:189]
	v_mfma_f32_32x32x16_bf16 v[174:189], v[166:169], v[88:91], v[174:189]
	v_mfma_f32_32x32x16_bf16 v[174:189], v[170:173], v[92:95], v[174:189]
	s_nop 11
	v_max3_f32 v200, v174, v175, v176
	v_max3_f32 v201, v177, v178, v179
	v_max3_f32 v202, v180, v181, v182
	v_max3_f32 v200, v200, v201, v202
	v_max3_f32 v201, v183, v184, v185
	v_max3_f32 v202, v186, v187, v188
	v_max3_f32 v201, v201, v202, v189
	v_max_f32_e32 v200, v200, v201
	v_mov_b32_e32 v201, v200
	s_nop 1
	v_permlane32_swap_b32_e32 v200, v201
	v_max_f32_e32 v201, v200, v201
	v_cmp_lt_f32_e32 vcc, 0, v201
	s_cbranch_vccz .Lfox_hot_2
	v_add_f32_e32 v201, v201, v154
	v_max3_f32 v205, v154, v201, s94
	v_sub_f32_e32 v204, v154, v205
	v_add_f32_e32 v174, v174, v204
	v_add_f32_e32 v175, v175, v204
	v_add_f32_e32 v176, v176, v204
	v_add_f32_e32 v177, v177, v204
	v_add_f32_e32 v178, v178, v204
	v_add_f32_e32 v179, v179, v204
	v_add_f32_e32 v180, v180, v204
	v_add_f32_e32 v181, v181, v204
	v_add_f32_e32 v182, v182, v204
	v_add_f32_e32 v183, v183, v204
	v_add_f32_e32 v184, v184, v204
	v_add_f32_e32 v185, v185, v204
	v_add_f32_e32 v186, v186, v204
	v_add_f32_e32 v187, v187, v204
	v_add_f32_e32 v188, v188, v204
	v_add_f32_e32 v189, v189, v204
	v_exp_f32_e32 v204, v204
	v_mov_b32_e32 v154, v205
	v_mul_f32_e32 v151, v151, v204
	v_pk_mul_f32 v[0:1], v[0:1], v[204:205] op_sel_hi:[1,0]
	v_pk_mul_f32 v[2:3], v[2:3], v[204:205] op_sel_hi:[1,0]
	v_pk_mul_f32 v[4:5], v[4:5], v[204:205] op_sel_hi:[1,0]
	v_pk_mul_f32 v[6:7], v[6:7], v[204:205] op_sel_hi:[1,0]
	v_pk_mul_f32 v[8:9], v[8:9], v[204:205] op_sel_hi:[1,0]
	v_pk_mul_f32 v[10:11], v[10:11], v[204:205] op_sel_hi:[1,0]
	v_pk_mul_f32 v[12:13], v[12:13], v[204:205] op_sel_hi:[1,0]
	v_pk_mul_f32 v[14:15], v[14:15], v[204:205] op_sel_hi:[1,0]
	v_pk_mul_f32 v[16:17], v[16:17], v[204:205] op_sel_hi:[1,0]
	v_pk_mul_f32 v[18:19], v[18:19], v[204:205] op_sel_hi:[1,0]
	v_pk_mul_f32 v[20:21], v[20:21], v[204:205] op_sel_hi:[1,0]
	v_pk_mul_f32 v[22:23], v[22:23], v[204:205] op_sel_hi:[1,0]
	v_pk_mul_f32 v[24:25], v[24:25], v[204:205] op_sel_hi:[1,0]
	v_pk_mul_f32 v[26:27], v[26:27], v[204:205] op_sel_hi:[1,0]
	v_pk_mul_f32 v[28:29], v[28:29], v[204:205] op_sel_hi:[1,0]
	v_pk_mul_f32 v[30:31], v[30:31], v[204:205] op_sel_hi:[1,0]
.Lfox_hot_2:
	v_exp_f32_e32 v174, v174
	v_exp_f32_e32 v175, v175
	v_exp_f32_e32 v176, v176
	v_exp_f32_e32 v177, v177
	v_add_f32_e32 v203, 0, v174
	v_exp_f32_e32 v178, v178
	v_add_f32_e32 v203, v175, v203
	v_exp_f32_e32 v179, v179
	v_add_f32_e32 v203, v176, v203
	v_exp_f32_e32 v180, v180
	v_add_f32_e32 v203, v177, v203
	v_exp_f32_e32 v181, v181
	v_add_f32_e32 v203, v178, v203
	v_exp_f32_e32 v182, v182
	v_add_f32_e32 v203, v179, v203
	v_exp_f32_e32 v183, v183
	v_add_f32_e32 v203, v180, v203
	v_exp_f32_e32 v184, v184
	v_add_f32_e32 v203, v181, v203
	v_exp_f32_e32 v185, v185
	v_cvt_pk_bf16_f32 v174, v174, v175
	v_cvt_pk_bf16_f32 v175, v176, v177
	v_cvt_pk_bf16_f32 v176, v178, v179
	v_cvt_pk_bf16_f32 v177, v180, v181
	v_add_f32_e32 v203, v182, v203
	v_exp_f32_e32 v186, v186
	s_waitcnt lgkmcnt(0)
	v_mfma_f32_32x32x16_bf16 v[0:15], v[108:111], v[174:177], v[0:15]
	v_add_f32_e32 v203, v183, v203
	v_exp_f32_e32 v187, v187
	v_add_f32_e32 v203, v184, v203
	v_exp_f32_e32 v188, v188
	v_add_f32_e32 v203, v185, v203
	v_exp_f32_e32 v189, v189
	v_mfma_f32_32x32x16_bf16 v[16:31], v[100:103], v[174:177], v[16:31]
	v_add_f32_e32 v203, v186, v203
	v_add_f32_e32 v203, v187, v203
	v_add_f32_e32 v203, v188, v203
	v_add_f32_e32 v203, v189, v203
	v_cvt_pk_bf16_f32 v178, v182, v183
	v_cvt_pk_bf16_f32 v179, v184, v185
	v_cvt_pk_bf16_f32 v180, v186, v187
	v_cvt_pk_bf16_f32 v181, v188, v189
	v_add_f32_e32 v151, v151, v203
	s_nop 0
	v_mfma_f32_32x32x16_bf16 v[0:15], v[104:107], v[178:181], v[0:15]
	v_mfma_f32_32x32x16_bf16 v[16:31], v[96:99], v[178:181], v[16:31]
	s_branch .LBB0_542
